# v89: v76 + conversion schedule: layer-1 expert down-projection weights converted beside layer 1's recurrence phase instead of in the prologue; layer-3 expert jobs re-split 3 ups / rest
# speedup vs baseline: 1.0034x; 1.0034x over previous
.LBB0_42:
	s_cmp_gt_u32 s18, 13
	s_cbranch_scc1 .LBB0_41
	s_cmp_lt_i32 s18, 3
	s_mov_b64 s[6:7], -1
	s_cbranch_scc1 .LBB0_60
	s_cmp_lt_i32 s18, 4
	s_cbranch_scc1 .LBB0_51
	s_cmp_lt_i32 s18, 5
	s_cbranch_scc1 .LBB0_52
	s_cmp_lg_u32 s18, 5
	s_cbranch_scc0 .LBB0_53
	s_cmp_gt_u32 s18, 13
	s_mov_b64 s[0:1], -1
	s_cbranch_scc0 .LBB0_49
	s_add_i32 s0, s18, -14
	v_readlane_b32 s36, v253, 34
	s_mul_i32 s2, s0, 0xe00000
	v_readlane_b32 s48, v253, 46
	s_mul_hi_u32 s1, s0, 0xe00000
	v_readlane_b32 s49, v253, 47
	s_add_u32 s2, s48, s2
	s_addc_u32 s3, s49, s1
	s_mul_hi_u32 s1, s0, 0x700000
	s_mul_i32 s0, s0, 0x700000
	v_readlane_b32 s4, v254, 21
	v_readlane_b32 s5, v254, 22
	s_add_u32 s4, s4, s0
	v_readlane_b32 s37, v253, 35
	v_readlane_b32 s38, v253, 36
	v_readlane_b32 s39, v253, 37
	v_readlane_b32 s40, v253, 38
	v_readlane_b32 s41, v253, 39
	v_readlane_b32 s42, v253, 40
	v_readlane_b32 s43, v253, 41
	v_readlane_b32 s44, v253, 42
	v_readlane_b32 s45, v253, 43
	v_readlane_b32 s46, v253, 44
	v_readlane_b32 s47, v253, 45
	v_readlane_b32 s50, v253, 48
	v_readlane_b32 s51, v253, 49
	s_addc_u32 s5, s5, s1
	s_mov_b64 s[0:1], 0

.LBB0_100:
	s_sub_i32 s0, s12, 18
	s_cmp_ge_u32 s0, 0
	s_cbranch_scc1 .LBB0_99
	s_add_i32 s3, s12, -14
	v_readlane_b32 s36, v253, 34
	s_mul_i32 s1, s3, 0xe00000
	v_readlane_b32 s48, v253, 46
	s_mul_hi_u32 s0, s3, 0xe00000
	v_readlane_b32 s49, v253, 47
	s_add_u32 s6, s48, s1
	s_addc_u32 s7, s49, s0
	s_abs_i32 s1, s10
	s_mul_hi_u32 s2, s1, s16
	s_mul_i32 s2, s2, s15
	s_sub_i32 s1, s1, s2
	s_ashr_i32 s0, s10, 31
	s_sub_i32 s2, s1, s15
	s_cmp_ge_u32 s1, s15
	s_cselect_b32 s1, s2, s1
	s_sub_i32 s2, s1, s15
	s_cmp_ge_u32 s1, s15
	s_cselect_b32 s1, s2, s1
	s_xor_b32 s1, s1, s0
	s_sub_i32 s0, s0, s1
	s_add_i32 s0, s14, s0
	s_ashr_i32 s1, s0, 31
	s_abs_i32 s0, s0
	s_mul_hi_u32 s2, s0, s16
	s_mul_i32 s2, s2, s15
	s_sub_i32 s0, s0, s2
	s_sub_i32 s2, s0, s15
	s_cmp_ge_u32 s0, s15
	s_cselect_b32 s0, s2, s0
	s_sub_i32 s2, s0, s15
	s_cmp_ge_u32 s0, s15
	s_cselect_b32 s0, s2, s0
	s_xor_b32 s0, s0, s1
	s_sub_i32 s13, s0, s1
	s_cmpk_lt_i32 s13, 0x700
	s_mov_b32 s17, 0
	s_cselect_b64 s[8:9], -1, 0
	s_cmpk_gt_i32 s13, 0x6ff
	s_mov_b32 s2, 0
	s_mov_b32 s0, 0
	v_readlane_b32 s37, v253, 35
	v_readlane_b32 s38, v253, 36
	v_readlane_b32 s39, v253, 37
	v_readlane_b32 s40, v253, 38
	v_readlane_b32 s41, v253, 39
	v_readlane_b32 s42, v253, 40
	v_readlane_b32 s43, v253, 41
	v_readlane_b32 s44, v253, 42
	v_readlane_b32 s45, v253, 43
	v_readlane_b32 s46, v253, 44
	v_readlane_b32 s47, v253, 45
	v_readlane_b32 s50, v253, 48
	v_readlane_b32 s51, v253, 49
	s_cbranch_scc0 .LBB0_104
	s_add_i32 s1, s13, s88
	s_cmpk_gt_i32 s1, 0x6ff
	s_mov_b32 s4, 0
	s_cbranch_scc0 .LBB0_105

.LBB0_1647:
	s_cmp_gt_u32 s21, 13
	s_cselect_b64 s[2:3], -1, 0
	s_cmp_lt_u32 s21, 31
	s_cselect_b32 s10, 1, 2
	s_cmp_lt_u32 s21, 22
	s_cselect_b64 s[0:1], -1, 0
	s_and_b64 s[8:9], s[0:1], exec
	s_cselect_b32 s8, 1, s10
	s_cmp_eq_u32 s8, s17
	s_cselect_b64 s[8:9], -1, 0
	s_and_b64 s[2:3], s[2:3], s[8:9]
	s_andn2_b64 vcc, exec, s[2:3]
	s_cbranch_vccnz .LBB0_1646
	s_cmp_gt_u32 s21, 21
	s_cselect_b64 s[8:9], -1, 0
	s_sub_i32 s2, s21, 22
	s_and_b64 s[0:1], s[0:1], exec
	s_cselect_b32 s26, s21, s2
	s_mov_b64 s[14:15], -1
	s_mov_b64 s[12:13], 0
	s_cmp_lt_i32 s26, 3
	s_mov_b64 s[10:11], 0
	s_cbranch_scc1 .LBB0_1660
	s_cmp_gt_i32 s26, 3
	s_cbranch_scc0 .LBB0_1654
	s_cmp_gt_i32 s26, 4
	s_cbranch_scc0 .LBB0_1655
	s_cmp_eq_u32 s26, 5
	s_mov_b64 s[10:11], -1
	s_cbranch_scc0 .LBB0_1653
	s_and_b64 s[0:1], s[8:9], exec
	s_cselect_b32 s2, 0x100000, 0
	v_readlane_b32 s48, v253, 34
	s_lshl_b32 s0, s2, 2
	v_readlane_b32 s54, v253, 40
	v_readlane_b32 s55, v253, 41
	s_add_u32 s0, s54, s0
	s_addc_u32 s1, s55, 0
	s_lshl_b32 s2, s2, 1
	v_readlane_b32 s10, v254, 9
	v_readlane_b32 s11, v254, 10
	s_add_u32 s2, s10, s2
	v_readlane_b32 s49, v253, 35
	v_readlane_b32 s50, v253, 36
	v_readlane_b32 s51, v253, 37
	v_readlane_b32 s52, v253, 38
	v_readlane_b32 s53, v253, 39
	v_readlane_b32 s56, v253, 42
	v_readlane_b32 s57, v253, 43
	v_readlane_b32 s58, v253, 44
	v_readlane_b32 s59, v253, 45
	v_readlane_b32 s60, v253, 46
	v_readlane_b32 s61, v253, 47
	v_readlane_b32 s62, v253, 48
	v_readlane_b32 s63, v253, 49
	s_addc_u32 s3, s11, 0
	s_mov_b64 s[10:11], 0

.LBB0_1710:
	s_cmp_gt_u32 s19, 13
	s_cselect_b64 s[2:3], -1, 0
	s_cmp_lt_u32 s19, 31
	s_cselect_b32 s10, 1, 2
	s_cmp_lt_u32 s19, 22
	s_cselect_b64 s[0:1], -1, 0
	s_and_b64 s[8:9], s[0:1], exec
	s_cselect_b32 s8, 1, s10
	s_cmp_eq_u32 s8, s17
	s_cselect_b64 s[8:9], -1, 0
	s_and_b64 s[2:3], s[2:3], s[8:9]
	s_andn2_b64 vcc, exec, s[2:3]
	s_cbranch_vccnz .LBB0_1709
	s_cmp_gt_u32 s19, 21
	s_cselect_b64 s[8:9], -1, 0
	s_sub_i32 s2, s19, 22
	s_and_b64 s[0:1], s[0:1], exec
	s_cselect_b32 s23, s19, s2
	s_mov_b64 s[14:15], -1
	s_mov_b64 s[12:13], 0
	s_cmp_lt_i32 s23, 3
	s_mov_b64 s[10:11], 0
	s_cbranch_scc1 .LBB0_1723
	s_cmp_gt_i32 s23, 3
	s_cbranch_scc0 .LBB0_1717
	s_cmp_gt_i32 s23, 4
	s_cbranch_scc0 .LBB0_1718
	s_cmp_eq_u32 s23, 5
	s_mov_b64 s[10:11], -1
	s_cbranch_scc0 .LBB0_1716
	s_and_b64 s[0:1], s[8:9], exec
	s_cselect_b32 s2, 0x100000, 0
	v_readlane_b32 s48, v253, 34
	s_lshl_b32 s0, s2, 2
	v_readlane_b32 s54, v253, 40
	v_readlane_b32 s55, v253, 41
	s_add_u32 s0, s54, s0
	s_addc_u32 s1, s55, 0
	s_lshl_b32 s2, s2, 1
	v_readlane_b32 s10, v254, 9
	v_readlane_b32 s11, v254, 10
	s_add_u32 s2, s10, s2
	v_readlane_b32 s49, v253, 35
	v_readlane_b32 s50, v253, 36
	v_readlane_b32 s51, v253, 37
	v_readlane_b32 s52, v253, 38
	v_readlane_b32 s53, v253, 39
	v_readlane_b32 s56, v253, 42
	v_readlane_b32 s57, v253, 43
	v_readlane_b32 s58, v253, 44
	v_readlane_b32 s59, v253, 45
	v_readlane_b32 s60, v253, 46
	v_readlane_b32 s61, v253, 47
	v_readlane_b32 s62, v253, 48
	v_readlane_b32 s63, v253, 49
	s_addc_u32 s3, s11, 0
	s_mov_b64 s[10:11], 0
